# speedup vs baseline: 1.0035x; 1.0015x over previous
.Lq2_nd0_1:
	v_mfma_scale_f32_32x32x64_f8f6f4 v[18:33], v[66:73], v[146:153], 0, v203, v203 op_sel_hi:[0,0,0]
	v_exp_f32_e64 v2, -v2
	v_exp_f32_e64 v3, -v3
	v_exp_f32_e64 v4, -v4
	v_exp_f32_e64 v5, -v5
	s_waitcnt lgkmcnt(0)
	v_add_co_u32_e64 v200, s[42:43], v200, v200
	v_add_co_u32_e64 v200, s[48:49], v200, v200
	v_add_co_u32_e64 v200, s[50:51], v200, v200
	v_add_co_u32_e64 v200, s[56:57], v200, v200
	v_pk_add_f32 v[2:3], v[2:3], v[162:163]
	v_pk_add_f32 v[4:5], v[4:5], v[164:165]
	s_mov_b64 exec, s[42:43]
	v_mul_f32_e32 v204, v204, v2
	s_mov_b64 exec, s[48:49]
	v_mul_f32_e32 v205, v205, v3
	s_mov_b64 exec, s[50:51]
	v_mul_f32_e32 v206, v206, v4
	s_mov_b64 exec, s[56:57]
	v_mul_f32_e32 v207, v207, v5
	s_mov_b64 exec, -1
	v_mfma_scale_f32_32x32x64_f8f6f4 v[18:33], v[74:81], v[154:161], v[18:33], v203, v203 op_sel_hi:[0,0,0]
	v_exp_f32_e64 v6, -v6
	v_exp_f32_e64 v7, -v7
	v_exp_f32_e64 v8, -v8
	v_exp_f32_e64 v9, -v9
	v_add_co_u32_e64 v200, s[42:43], v200, v200
	v_add_co_u32_e64 v200, s[48:49], v200, v200
	v_add_co_u32_e64 v200, s[50:51], v200, v200
	v_add_co_u32_e64 v200, s[56:57], v200, v200
	v_pk_add_f32 v[6:7], v[6:7], v[166:167]
	v_pk_add_f32 v[8:9], v[8:9], v[168:169]
	s_mov_b64 exec, s[42:43]
	v_mul_f32_e32 v208, v208, v6
	s_mov_b64 exec, s[48:49]
	v_mul_f32_e32 v209, v209, v7
	s_mov_b64 exec, s[50:51]
	v_mul_f32_e32 v210, v210, v8
	s_mov_b64 exec, s[56:57]
	v_mul_f32_e32 v211, v211, v9
	s_mov_b64 exec, -1
	v_mfma_scale_f32_32x32x64_f8f6f4 v[18:33], v[82:89], v[138:145], v[18:33], v203, v203 op_sel_hi:[0,0,0]
	v_exp_f32_e64 v10, -v10
	v_exp_f32_e64 v11, -v11
	v_exp_f32_e64 v12, -v12
	v_exp_f32_e64 v13, -v13
	v_add_co_u32_e64 v200, s[42:43], v200, v200
	v_add_co_u32_e64 v200, s[48:49], v200, v200
	v_add_co_u32_e64 v200, s[50:51], v200, v200
	v_add_co_u32_e64 v200, s[56:57], v200, v200
	v_pk_add_f32 v[10:11], v[10:11], v[170:171]
	v_pk_add_f32 v[12:13], v[12:13], v[172:173]
	s_mov_b64 exec, s[42:43]
	v_mul_f32_e32 v212, v212, v10
	s_mov_b64 exec, s[48:49]
	v_mul_f32_e32 v213, v213, v11
	s_mov_b64 exec, s[50:51]
	v_mul_f32_e32 v214, v214, v12
	s_mov_b64 exec, s[56:57]
	v_mul_f32_e32 v215, v215, v13
	s_mov_b64 exec, -1
	v_mfma_scale_f32_32x32x64_f8f6f4 v[18:33], v[90:97], v[130:137], v[18:33], v203, v203 op_sel_hi:[0,0,0]
	v_exp_f32_e64 v14, -v14
	v_exp_f32_e64 v15, -v15
	v_exp_f32_e64 v16, -v16
	v_exp_f32_e64 v17, -v17
	v_add_co_u32_e64 v200, s[42:43], v200, v200
	v_add_co_u32_e64 v200, s[48:49], v200, v200
	v_add_co_u32_e64 v200, s[50:51], v200, v200
	v_add_co_u32_e64 v200, s[56:57], v200, v200
	v_pk_add_f32 v[14:15], v[14:15], v[174:175]
	v_pk_add_f32 v[16:17], v[16:17], v[176:177]
	s_mov_b64 exec, s[42:43]
	v_mul_f32_e32 v216, v216, v14
	s_mov_b64 exec, s[48:49]
	v_mul_f32_e32 v217, v217, v15
	s_mov_b64 exec, s[50:51]
	v_mul_f32_e32 v218, v218, v16
	s_mov_b64 exec, s[56:57]
	v_mul_f32_e32 v219, v219, v17
	s_mov_b64 exec, -1
	s_cmp_lg_u32 s55, s40
	s_cbranch_scc1 .Lq2_nd1_1
	s_nop 15
	s_nop 7
	v_cndmask_b32_e64 v18, v18, v199, s[0:1]
	v_cndmask_b32_e64 v19, v19, v199, s[2:3]
	v_cndmask_b32_e64 v20, v20, v199, s[4:5]
	v_cndmask_b32_e64 v21, v21, v199, s[6:7]
	v_cndmask_b32_e64 v22, v22, v199, s[8:9]
	v_cndmask_b32_e64 v23, v23, v199, s[10:11]
	v_cndmask_b32_e64 v24, v24, v199, s[12:13]
	v_cndmask_b32_e64 v25, v25, v199, s[14:15]
	v_cndmask_b32_e64 v26, v26, v199, s[16:17]
	v_cndmask_b32_e64 v27, v27, v199, s[18:19]
	v_cndmask_b32_e64 v28, v28, v199, s[20:21]
	v_cndmask_b32_e64 v29, v29, v199, s[22:23]
	v_cndmask_b32_e64 v30, v30, v199, s[24:25]
	v_cndmask_b32_e64 v31, v31, v199, s[26:27]
	v_cndmask_b32_e64 v32, v32, v199, s[28:29]
	v_cndmask_b32_e64 v33, v33, v199, s[30:31]
.Lq2_nd1_1:
	s_nop 3
	s_waitcnt vmcnt(6)
	v_mfma_scale_f32_32x32x64_f8f6f4 v[2:17], v[34:41], v[106:113], 0, v203, v203 op_sel_hi:[0,0,0]
	v_exp_f32_e64 v18, -v18
	v_exp_f32_e64 v19, -v19
	v_exp_f32_e64 v20, -v20
	v_exp_f32_e64 v21, -v21
	v_add_co_u32_e64 v200, s[42:43], v200, v200
	v_add_co_u32_e64 v200, s[48:49], v200, v200
	v_add_co_u32_e64 v200, s[50:51], v200, v200
	v_add_co_u32_e64 v200, s[56:57], v200, v200
	v_pk_add_f32 v[18:19], v[18:19], v[178:179]
	v_pk_add_f32 v[20:21], v[20:21], v[180:181]
	s_mov_b64 exec, s[42:43]
	v_mul_f32_e32 v220, v220, v18
	s_mov_b64 exec, s[48:49]
	v_mul_f32_e32 v221, v221, v19
	s_mov_b64 exec, s[50:51]
	v_mul_f32_e32 v222, v222, v20
	s_mov_b64 exec, s[56:57]
	v_mul_f32_e32 v223, v223, v21
	s_mov_b64 exec, -1
	s_waitcnt vmcnt(4)
	v_mfma_scale_f32_32x32x64_f8f6f4 v[2:17], v[42:49], v[122:129], v[2:17], v203, v203 op_sel_hi:[0,0,0]
	v_exp_f32_e64 v22, -v22
	v_exp_f32_e64 v23, -v23
	v_exp_f32_e64 v24, -v24
	v_exp_f32_e64 v25, -v25
	v_add_co_u32_e64 v200, s[42:43], v200, v200
	v_add_co_u32_e64 v200, s[48:49], v200, v200
	v_add_co_u32_e64 v200, s[50:51], v200, v200
	v_add_co_u32_e64 v200, s[56:57], v200, v200
	v_pk_add_f32 v[22:23], v[22:23], v[182:183]
	v_pk_add_f32 v[24:25], v[24:25], v[184:185]
	s_mov_b64 exec, s[42:43]
	v_mul_f32_e32 v224, v224, v22
	s_mov_b64 exec, s[48:49]
	v_mul_f32_e32 v225, v225, v23
	s_mov_b64 exec, s[50:51]
	v_mul_f32_e32 v226, v226, v24
	s_mov_b64 exec, s[56:57]
	v_mul_f32_e32 v227, v227, v25
	s_mov_b64 exec, -1
	s_waitcnt vmcnt(2)
	v_mfma_scale_f32_32x32x64_f8f6f4 v[2:17], v[50:57], v[114:121], v[2:17], v203, v203 op_sel_hi:[0,0,0]
	v_exp_f32_e64 v26, -v26
	v_exp_f32_e64 v27, -v27
	v_exp_f32_e64 v28, -v28
	v_exp_f32_e64 v29, -v29
	v_add_co_u32_e64 v200, s[42:43], v200, v200
	v_add_co_u32_e64 v200, s[48:49], v200, v200
	v_add_co_u32_e64 v200, s[50:51], v200, v200
	v_add_co_u32_e64 v200, s[56:57], v200, v200
	v_pk_add_f32 v[26:27], v[26:27], v[186:187]
	v_pk_add_f32 v[28:29], v[28:29], v[188:189]
	s_mov_b64 exec, s[42:43]
	v_mul_f32_e32 v228, v228, v26
	s_mov_b64 exec, s[48:49]
	v_mul_f32_e32 v229, v229, v27
	s_mov_b64 exec, s[50:51]
	v_mul_f32_e32 v230, v230, v28
	s_mov_b64 exec, s[56:57]
	v_mul_f32_e32 v231, v231, v29
	s_mov_b64 exec, -1
	s_waitcnt vmcnt(0)
	v_mfma_scale_f32_32x32x64_f8f6f4 v[2:17], v[58:65], v[98:105], v[2:17], v203, v203 op_sel_hi:[0,0,0]
	v_exp_f32_e64 v30, -v30
	v_exp_f32_e64 v31, -v31
	v_exp_f32_e64 v32, -v32
	v_exp_f32_e64 v33, -v33
	v_add_co_u32_e64 v200, s[42:43], v200, v200
	v_add_co_u32_e64 v200, s[48:49], v200, v200
	v_add_co_u32_e64 v200, s[50:51], v200, v200
	v_add_co_u32_e64 v200, s[56:57], v200, v200
	v_pk_add_f32 v[30:31], v[30:31], v[190:191]
	v_pk_add_f32 v[32:33], v[32:33], v[192:193]
	s_mov_b64 exec, s[42:43]
	v_mul_f32_e32 v232, v232, v30
	s_mov_b64 exec, s[48:49]
	v_mul_f32_e32 v233, v233, v31
	s_mov_b64 exec, s[50:51]
	v_mul_f32_e32 v234, v234, v32
	s_mov_b64 exec, s[56:57]
	v_mul_f32_e32 v235, v235, v33
	s_mov_b64 exec, -1
	s_lshl_b32 s34, s39, 2
	s_add_i32 s34, s34, 2
	s_add_i32 s34, s34, s35
	s_and_b32 s41, s34, 15
	s_add_i32 s54, s34, 1
	s_and_b32 s54, s54, 15
	s_lshl_b32 s55, s41, 8
	s_lshl_b32 s38, s52, 12
	s_add_i32 s55, s55, s38
	v_lshl_add_u32 v236, v194, 2, s55
	ds_read_b32 v200, v236
	s_lshl_b32 s34, s54, 3
	s_add_i32 s34, s34, s52
	s_lshl_b32 s34, s34, 13
	s_add_i32 s34, s34, s53
	buffer_load_dwordx4 v[146:149], v195, s[44:47], s34 offen
	s_or_b32 s42, s34, 0x400
	buffer_load_dwordx4 v[150:153], v195, s[44:47], s42 offen
	s_or_b32 s43, s34, 0x800
	buffer_load_dwordx4 v[154:157], v195, s[44:47], s43 offen
	s_or_b32 s42, s34, 0xc00
	buffer_load_dwordx4 v[158:161], v195, s[44:47], s42 offen
	s_or_b32 s43, s34, 0x1000
	buffer_load_dwordx4 v[138:141], v195, s[44:47], s43 offen
	s_or_b32 s42, s34, 0x1400
	buffer_load_dwordx4 v[142:145], v195, s[44:47], s42 offen
	s_or_b32 s43, s34, 0x1800
	buffer_load_dwordx4 v[130:133], v195, s[44:47], s43 offen
	s_or_b32 s42, s34, 0x1c00
	buffer_load_dwordx4 v[134:137], v195, s[44:47], s42 offen
	s_lshl_b32 s55, s41, 3
	s_add_i32 s55, s55, s52
	s_cmp_lg_u32 s55, s33
	s_cbranch_scc1 .Lq2_nd0_2
	v_cndmask_b32_e64 v2, v2, v198, s[0:1]
	v_cndmask_b32_e64 v3, v3, v198, s[2:3]
	v_cndmask_b32_e64 v4, v4, v198, s[4:5]
	v_cndmask_b32_e64 v5, v5, v198, s[6:7]
	v_cndmask_b32_e64 v6, v6, v198, s[8:9]
	v_cndmask_b32_e64 v7, v7, v198, s[10:11]
	v_cndmask_b32_e64 v8, v8, v198, s[12:13]
	v_cndmask_b32_e64 v9, v9, v198, s[14:15]
	v_cndmask_b32_e64 v10, v10, v198, s[16:17]
	v_cndmask_b32_e64 v11, v11, v198, s[18:19]
	v_cndmask_b32_e64 v12, v12, v198, s[20:21]
	v_cndmask_b32_e64 v13, v13, v198, s[22:23]
	v_cndmask_b32_e64 v14, v14, v198, s[24:25]
	v_cndmask_b32_e64 v15, v15, v198, s[26:27]
	v_cndmask_b32_e64 v16, v16, v198, s[28:29]
	v_cndmask_b32_e64 v17, v17, v198, s[30:31]
.Lq2_nd0_2:
	v_mfma_scale_f32_32x32x64_f8f6f4 v[18:33], v[66:73], v[106:113], 0, v203, v203 op_sel_hi:[0,0,0]
	v_exp_f32_e64 v2, -v2
	v_exp_f32_e64 v3, -v3
	v_exp_f32_e64 v4, -v4
	v_exp_f32_e64 v5, -v5
	s_waitcnt lgkmcnt(0)
	v_add_co_u32_e64 v200, s[42:43], v200, v200
	v_add_co_u32_e64 v200, s[48:49], v200, v200
	v_add_co_u32_e64 v200, s[50:51], v200, v200
	v_add_co_u32_e64 v200, s[56:57], v200, v200
	v_pk_add_f32 v[2:3], v[2:3], v[162:163]
	v_pk_add_f32 v[4:5], v[4:5], v[164:165]
	s_mov_b64 exec, s[42:43]
	v_mul_f32_e32 v204, v204, v2
	s_mov_b64 exec, s[48:49]
	v_mul_f32_e32 v205, v205, v3
	s_mov_b64 exec, s[50:51]
	v_mul_f32_e32 v206, v206, v4
	s_mov_b64 exec, s[56:57]
	v_mul_f32_e32 v207, v207, v5
	s_mov_b64 exec, -1
	v_mfma_scale_f32_32x32x64_f8f6f4 v[18:33], v[74:81], v[122:129], v[18:33], v203, v203 op_sel_hi:[0,0,0]
	v_exp_f32_e64 v6, -v6
	v_exp_f32_e64 v7, -v7
	v_exp_f32_e64 v8, -v8
	v_exp_f32_e64 v9, -v9
	v_add_co_u32_e64 v200, s[42:43], v200, v200
	v_add_co_u32_e64 v200, s[48:49], v200, v200
	v_add_co_u32_e64 v200, s[50:51], v200, v200
	v_add_co_u32_e64 v200, s[56:57], v200, v200
	v_pk_add_f32 v[6:7], v[6:7], v[166:167]
	v_pk_add_f32 v[8:9], v[8:9], v[168:169]
	s_mov_b64 exec, s[42:43]
	v_mul_f32_e32 v208, v208, v6
	s_mov_b64 exec, s[48:49]
	v_mul_f32_e32 v209, v209, v7
	s_mov_b64 exec, s[50:51]
	v_mul_f32_e32 v210, v210, v8
	s_mov_b64 exec, s[56:57]
	v_mul_f32_e32 v211, v211, v9
	s_mov_b64 exec, -1
	v_mfma_scale_f32_32x32x64_f8f6f4 v[18:33], v[82:89], v[114:121], v[18:33], v203, v203 op_sel_hi:[0,0,0]
	v_exp_f32_e64 v10, -v10
	v_exp_f32_e64 v11, -v11
	v_exp_f32_e64 v12, -v12
	v_exp_f32_e64 v13, -v13
	v_add_co_u32_e64 v200, s[42:43], v200, v200
	v_add_co_u32_e64 v200, s[48:49], v200, v200
	v_add_co_u32_e64 v200, s[50:51], v200, v200
	v_add_co_u32_e64 v200, s[56:57], v200, v200
	v_pk_add_f32 v[10:11], v[10:11], v[170:171]
	v_pk_add_f32 v[12:13], v[12:13], v[172:173]
	s_mov_b64 exec, s[42:43]
	v_mul_f32_e32 v212, v212, v10
	s_mov_b64 exec, s[48:49]
	v_mul_f32_e32 v213, v213, v11
	s_mov_b64 exec, s[50:51]
	v_mul_f32_e32 v214, v214, v12
	s_mov_b64 exec, s[56:57]
	v_mul_f32_e32 v215, v215, v13
	s_mov_b64 exec, -1
	v_mfma_scale_f32_32x32x64_f8f6f4 v[18:33], v[90:97], v[98:105], v[18:33], v203, v203 op_sel_hi:[0,0,0]
	v_exp_f32_e64 v14, -v14
	v_exp_f32_e64 v15, -v15
	v_exp_f32_e64 v16, -v16
	v_exp_f32_e64 v17, -v17
	v_add_co_u32_e64 v200, s[42:43], v200, v200
	v_add_co_u32_e64 v200, s[48:49], v200, v200
	v_add_co_u32_e64 v200, s[50:51], v200, v200
	v_add_co_u32_e64 v200, s[56:57], v200, v200
	v_pk_add_f32 v[14:15], v[14:15], v[174:175]
	v_pk_add_f32 v[16:17], v[16:17], v[176:177]
	s_mov_b64 exec, s[42:43]
	v_mul_f32_e32 v216, v216, v14
	s_mov_b64 exec, s[48:49]
	v_mul_f32_e32 v217, v217, v15
	s_mov_b64 exec, s[50:51]
	v_mul_f32_e32 v218, v218, v16
	s_mov_b64 exec, s[56:57]
	v_mul_f32_e32 v219, v219, v17
	s_mov_b64 exec, -1
	s_cmp_lg_u32 s55, s40
	s_cbranch_scc1 .Lq2_nd1_2
	s_nop 15
	s_nop 7
	v_cndmask_b32_e64 v18, v18, v199, s[0:1]
	v_cndmask_b32_e64 v19, v19, v199, s[2:3]
	v_cndmask_b32_e64 v20, v20, v199, s[4:5]
	v_cndmask_b32_e64 v21, v21, v199, s[6:7]
	v_cndmask_b32_e64 v22, v22, v199, s[8:9]
	v_cndmask_b32_e64 v23, v23, v199, s[10:11]
	v_cndmask_b32_e64 v24, v24, v199, s[12:13]
	v_cndmask_b32_e64 v25, v25, v199, s[14:15]
	v_cndmask_b32_e64 v26, v26, v199, s[16:17]
	v_cndmask_b32_e64 v27, v27, v199, s[18:19]
	v_cndmask_b32_e64 v28, v28, v199, s[20:21]
	v_cndmask_b32_e64 v29, v29, v199, s[22:23]
	v_cndmask_b32_e64 v30, v30, v199, s[24:25]
	v_cndmask_b32_e64 v31, v31, v199, s[26:27]
	v_cndmask_b32_e64 v32, v32, v199, s[28:29]
	v_cndmask_b32_e64 v33, v33, v199, s[30:31]
.Lq2_nd1_2:
	s_nop 3
	s_waitcnt vmcnt(6)
	v_mfma_scale_f32_32x32x64_f8f6f4 v[2:17], v[34:41], v[146:153], 0, v203, v203 op_sel_hi:[0,0,0]
	v_exp_f32_e64 v18, -v18
	v_exp_f32_e64 v19, -v19
	v_exp_f32_e64 v20, -v20
	v_exp_f32_e64 v21, -v21
	v_add_co_u32_e64 v200, s[42:43], v200, v200
	v_add_co_u32_e64 v200, s[48:49], v200, v200
	v_add_co_u32_e64 v200, s[50:51], v200, v200
	v_add_co_u32_e64 v200, s[56:57], v200, v200
	v_pk_add_f32 v[18:19], v[18:19], v[178:179]
	v_pk_add_f32 v[20:21], v[20:21], v[180:181]
	s_mov_b64 exec, s[42:43]
	v_mul_f32_e32 v220, v220, v18
	s_mov_b64 exec, s[48:49]
	v_mul_f32_e32 v221, v221, v19
	s_mov_b64 exec, s[50:51]
	v_mul_f32_e32 v222, v222, v20
	s_mov_b64 exec, s[56:57]
	v_mul_f32_e32 v223, v223, v21
	s_mov_b64 exec, -1
	s_waitcnt vmcnt(4)
	v_mfma_scale_f32_32x32x64_f8f6f4 v[2:17], v[42:49], v[154:161], v[2:17], v203, v203 op_sel_hi:[0,0,0]
	v_exp_f32_e64 v22, -v22
	v_exp_f32_e64 v23, -v23
	v_exp_f32_e64 v24, -v24
	v_exp_f32_e64 v25, -v25
	v_add_co_u32_e64 v200, s[42:43], v200, v200
	v_add_co_u32_e64 v200, s[48:49], v200, v200
	v_add_co_u32_e64 v200, s[50:51], v200, v200
	v_add_co_u32_e64 v200, s[56:57], v200, v200
	v_pk_add_f32 v[22:23], v[22:23], v[182:183]
	v_pk_add_f32 v[24:25], v[24:25], v[184:185]
	s_mov_b64 exec, s[42:43]
	v_mul_f32_e32 v224, v224, v22
	s_mov_b64 exec, s[48:49]
	v_mul_f32_e32 v225, v225, v23
	s_mov_b64 exec, s[50:51]
	v_mul_f32_e32 v226, v226, v24
	s_mov_b64 exec, s[56:57]
	v_mul_f32_e32 v227, v227, v25
	s_mov_b64 exec, -1
	s_waitcnt vmcnt(2)
	v_mfma_scale_f32_32x32x64_f8f6f4 v[2:17], v[50:57], v[138:145], v[2:17], v203, v203 op_sel_hi:[0,0,0]
	v_exp_f32_e64 v26, -v26
	v_exp_f32_e64 v27, -v27
	v_exp_f32_e64 v28, -v28
	v_exp_f32_e64 v29, -v29
	v_add_co_u32_e64 v200, s[42:43], v200, v200
	v_add_co_u32_e64 v200, s[48:49], v200, v200
	v_add_co_u32_e64 v200, s[50:51], v200, v200
	v_add_co_u32_e64 v200, s[56:57], v200, v200
	v_pk_add_f32 v[26:27], v[26:27], v[186:187]
	v_pk_add_f32 v[28:29], v[28:29], v[188:189]
	s_mov_b64 exec, s[42:43]
	v_mul_f32_e32 v228, v228, v26
	s_mov_b64 exec, s[48:49]
	v_mul_f32_e32 v229, v229, v27
	s_mov_b64 exec, s[50:51]
	v_mul_f32_e32 v230, v230, v28
	s_mov_b64 exec, s[56:57]
	v_mul_f32_e32 v231, v231, v29
	s_mov_b64 exec, -1
	s_waitcnt vmcnt(0)
	v_mfma_scale_f32_32x32x64_f8f6f4 v[2:17], v[58:65], v[130:137], v[2:17], v203, v203 op_sel_hi:[0,0,0]
	v_exp_f32_e64 v30, -v30
	v_exp_f32_e64 v31, -v31
	v_exp_f32_e64 v32, -v32
	v_exp_f32_e64 v33, -v33
	v_add_co_u32_e64 v200, s[42:43], v200, v200
	v_add_co_u32_e64 v200, s[48:49], v200, v200
	v_add_co_u32_e64 v200, s[50:51], v200, v200
	v_add_co_u32_e64 v200, s[56:57], v200, v200
	v_pk_add_f32 v[30:31], v[30:31], v[190:191]
	v_pk_add_f32 v[32:33], v[32:33], v[192:193]
	s_mov_b64 exec, s[42:43]
	v_mul_f32_e32 v232, v232, v30
	s_mov_b64 exec, s[48:49]
	v_mul_f32_e32 v233, v233, v31
	s_mov_b64 exec, s[50:51]
	v_mul_f32_e32 v234, v234, v32
	s_mov_b64 exec, s[56:57]
	v_mul_f32_e32 v235, v235, v33
	s_mov_b64 exec, -1
	s_lshl_b32 s34, s39, 2
	s_add_i32 s34, s34, 3
	s_add_i32 s34, s34, s35
	s_and_b32 s41, s34, 15
	s_add_i32 s54, s34, 1
	s_and_b32 s54, s54, 15
	s_lshl_b32 s55, s41, 8
	s_lshl_b32 s38, s52, 12
	s_add_i32 s55, s55, s38
	v_lshl_add_u32 v236, v194, 2, s55
	ds_read_b32 v200, v236
	s_cmp_eq_u32 s39, 3
	s_cbranch_scc1 .Lq2_nobl
	s_lshl_b32 s34, s54, 3
	s_add_i32 s34, s34, s52
	s_lshl_b32 s34, s34, 13
	s_add_i32 s34, s34, s53
	buffer_load_dwordx4 v[106:109], v195, s[44:47], s34 offen
	s_or_b32 s42, s34, 0x400
	buffer_load_dwordx4 v[110:113], v195, s[44:47], s42 offen
	s_or_b32 s43, s34, 0x800
	buffer_load_dwordx4 v[122:125], v195, s[44:47], s43 offen
	s_or_b32 s42, s34, 0xc00
	buffer_load_dwordx4 v[126:129], v195, s[44:47], s42 offen
	s_or_b32 s43, s34, 0x1000
	buffer_load_dwordx4 v[114:117], v195, s[44:47], s43 offen
	s_or_b32 s42, s34, 0x1400
	buffer_load_dwordx4 v[118:121], v195, s[44:47], s42 offen
	s_or_b32 s43, s34, 0x1800
	buffer_load_dwordx4 v[98:101], v195, s[44:47], s43 offen
	s_or_b32 s42, s34, 0x1c00
	buffer_load_dwordx4 v[102:105], v195, s[44:47], s42 offen

.Lq2_nd0_3:
	v_mfma_scale_f32_32x32x64_f8f6f4 v[18:33], v[66:73], v[146:153], 0, v203, v203 op_sel_hi:[0,0,0]
	ds_read_b128 v[236:239], v202
	v_exp_f32_e64 v2, -v2
	v_exp_f32_e64 v3, -v3
	v_exp_f32_e64 v4, -v4
	v_exp_f32_e64 v5, -v5
	s_waitcnt lgkmcnt(1)
	v_add_co_u32_e64 v200, s[42:43], v200, v200
	v_add_co_u32_e64 v200, s[48:49], v200, v200
	v_add_co_u32_e64 v200, s[50:51], v200, v200
	v_add_co_u32_e64 v200, s[56:57], v200, v200
	v_pk_add_f32 v[2:3], v[2:3], v[162:163]
	v_pk_add_f32 v[4:5], v[4:5], v[164:165]
	s_mov_b64 exec, s[42:43]
	v_mul_f32_e32 v204, v204, v2
	s_mov_b64 exec, s[48:49]
	v_mul_f32_e32 v205, v205, v3
	s_mov_b64 exec, s[50:51]
	v_mul_f32_e32 v206, v206, v4
	s_mov_b64 exec, s[56:57]
	v_mul_f32_e32 v207, v207, v5
	s_mov_b64 exec, -1
	v_log_f32_e32 v2, v204
	v_log_f32_e32 v3, v205
	v_log_f32_e32 v4, v206
	v_log_f32_e32 v5, v207
	s_waitcnt lgkmcnt(0)
	v_pk_fma_f32 v[0:1], v[2:3], v[236:237], v[0:1]
	v_pk_fma_f32 v[0:1], v[4:5], v[238:239], v[0:1]
	v_mfma_scale_f32_32x32x64_f8f6f4 v[18:33], v[74:81], v[154:161], v[18:33], v203, v203 op_sel_hi:[0,0,0]
	ds_read_b128 v[236:239], v202 offset:16
	v_exp_f32_e64 v6, -v6
	v_exp_f32_e64 v7, -v7
	v_exp_f32_e64 v8, -v8
	v_exp_f32_e64 v9, -v9
	v_add_co_u32_e64 v200, s[42:43], v200, v200
	v_add_co_u32_e64 v200, s[48:49], v200, v200
	v_add_co_u32_e64 v200, s[50:51], v200, v200
	v_add_co_u32_e64 v200, s[56:57], v200, v200
	v_pk_add_f32 v[6:7], v[6:7], v[166:167]
	v_pk_add_f32 v[8:9], v[8:9], v[168:169]
	s_mov_b64 exec, s[42:43]
	v_mul_f32_e32 v208, v208, v6
	s_mov_b64 exec, s[48:49]
	v_mul_f32_e32 v209, v209, v7
	s_mov_b64 exec, s[50:51]
	v_mul_f32_e32 v210, v210, v8
	s_mov_b64 exec, s[56:57]
	v_mul_f32_e32 v211, v211, v9
	s_mov_b64 exec, -1
	v_log_f32_e32 v6, v208
	v_log_f32_e32 v7, v209
	v_log_f32_e32 v8, v210
	v_log_f32_e32 v9, v211
	s_waitcnt lgkmcnt(0)
	v_pk_fma_f32 v[0:1], v[6:7], v[236:237], v[0:1]
	v_pk_fma_f32 v[0:1], v[8:9], v[238:239], v[0:1]
	v_mfma_scale_f32_32x32x64_f8f6f4 v[18:33], v[82:89], v[138:145], v[18:33], v203, v203 op_sel_hi:[0,0,0]
	ds_read_b128 v[236:239], v202 offset:32
	v_exp_f32_e64 v10, -v10
	v_exp_f32_e64 v11, -v11
	v_exp_f32_e64 v12, -v12
	v_exp_f32_e64 v13, -v13
	v_add_co_u32_e64 v200, s[42:43], v200, v200
	v_add_co_u32_e64 v200, s[48:49], v200, v200
	v_add_co_u32_e64 v200, s[50:51], v200, v200
	v_add_co_u32_e64 v200, s[56:57], v200, v200
	v_pk_add_f32 v[10:11], v[10:11], v[170:171]
	v_pk_add_f32 v[12:13], v[12:13], v[172:173]
	s_mov_b64 exec, s[42:43]
	v_mul_f32_e32 v212, v212, v10
	s_mov_b64 exec, s[48:49]
	v_mul_f32_e32 v213, v213, v11
	s_mov_b64 exec, s[50:51]
	v_mul_f32_e32 v214, v214, v12
	s_mov_b64 exec, s[56:57]
	v_mul_f32_e32 v215, v215, v13
	s_mov_b64 exec, -1
	v_log_f32_e32 v10, v212
	v_log_f32_e32 v11, v213
	v_log_f32_e32 v12, v214
	v_log_f32_e32 v13, v215
	s_waitcnt lgkmcnt(0)
	v_pk_fma_f32 v[0:1], v[10:11], v[236:237], v[0:1]
	v_pk_fma_f32 v[0:1], v[12:13], v[238:239], v[0:1]
	v_mfma_scale_f32_32x32x64_f8f6f4 v[18:33], v[90:97], v[130:137], v[18:33], v203, v203 op_sel_hi:[0,0,0]
	ds_read_b128 v[236:239], v202 offset:48
	v_exp_f32_e64 v14, -v14
	v_exp_f32_e64 v15, -v15
	v_exp_f32_e64 v16, -v16
	v_exp_f32_e64 v17, -v17
	v_add_co_u32_e64 v200, s[42:43], v200, v200
	v_add_co_u32_e64 v200, s[48:49], v200, v200
	v_add_co_u32_e64 v200, s[50:51], v200, v200
	v_add_co_u32_e64 v200, s[56:57], v200, v200
	v_pk_add_f32 v[14:15], v[14:15], v[174:175]
	v_pk_add_f32 v[16:17], v[16:17], v[176:177]
	s_mov_b64 exec, s[42:43]
	v_mul_f32_e32 v216, v216, v14
	s_mov_b64 exec, s[48:49]
	v_mul_f32_e32 v217, v217, v15
	s_mov_b64 exec, s[50:51]
	v_mul_f32_e32 v218, v218, v16
	s_mov_b64 exec, s[56:57]
	v_mul_f32_e32 v219, v219, v17
	s_mov_b64 exec, -1
	v_log_f32_e32 v14, v216
	v_log_f32_e32 v15, v217
	v_log_f32_e32 v16, v218
	v_log_f32_e32 v17, v219
	s_waitcnt lgkmcnt(0)
	v_pk_fma_f32 v[0:1], v[14:15], v[236:237], v[0:1]
	v_pk_fma_f32 v[0:1], v[16:17], v[238:239], v[0:1]
	s_cmp_lg_u32 s55, s40
	s_cbranch_scc1 .Lq2_nd1_3
	s_nop 15
	s_nop 7
	v_cndmask_b32_e64 v18, v18, v199, s[0:1]
	v_cndmask_b32_e64 v19, v19, v199, s[2:3]
	v_cndmask_b32_e64 v20, v20, v199, s[4:5]
	v_cndmask_b32_e64 v21, v21, v199, s[6:7]
	v_cndmask_b32_e64 v22, v22, v199, s[8:9]
	v_cndmask_b32_e64 v23, v23, v199, s[10:11]
	v_cndmask_b32_e64 v24, v24, v199, s[12:13]
	v_cndmask_b32_e64 v25, v25, v199, s[14:15]
	v_cndmask_b32_e64 v26, v26, v199, s[16:17]
	v_cndmask_b32_e64 v27, v27, v199, s[18:19]
	v_cndmask_b32_e64 v28, v28, v199, s[20:21]
	v_cndmask_b32_e64 v29, v29, v199, s[22:23]
	v_cndmask_b32_e64 v30, v30, v199, s[24:25]
	v_cndmask_b32_e64 v31, v31, v199, s[26:27]
	v_cndmask_b32_e64 v32, v32, v199, s[28:29]
	v_cndmask_b32_e64 v33, v33, v199, s[30:31]
.Lq2_nd1_3:
	s_nop 3
	s_cmp_eq_u32 s39, 3
	s_cbranch_scc1 .Lq2_lasthalf
	s_waitcnt vmcnt(6)
	v_mfma_scale_f32_32x32x64_f8f6f4 v[2:17], v[34:41], v[106:113], 0, v203, v203 op_sel_hi:[0,0,0]
	ds_read_b128 v[236:239], v202 offset:64
	v_exp_f32_e64 v18, -v18
	v_exp_f32_e64 v19, -v19
	v_exp_f32_e64 v20, -v20
	v_exp_f32_e64 v21, -v21
	v_add_co_u32_e64 v200, s[42:43], v200, v200
	v_add_co_u32_e64 v200, s[48:49], v200, v200
	v_add_co_u32_e64 v200, s[50:51], v200, v200
	v_add_co_u32_e64 v200, s[56:57], v200, v200
	v_pk_add_f32 v[18:19], v[18:19], v[178:179]
	v_pk_add_f32 v[20:21], v[20:21], v[180:181]
	s_mov_b64 exec, s[42:43]
	v_mul_f32_e32 v220, v220, v18
	s_mov_b64 exec, s[48:49]
	v_mul_f32_e32 v221, v221, v19
	s_mov_b64 exec, s[50:51]
	v_mul_f32_e32 v222, v222, v20
	s_mov_b64 exec, s[56:57]
	v_mul_f32_e32 v223, v223, v21
	s_mov_b64 exec, -1
	v_log_f32_e32 v18, v220
	v_log_f32_e32 v19, v221
	v_log_f32_e32 v20, v222
	v_log_f32_e32 v21, v223
	s_waitcnt lgkmcnt(0)
	v_pk_fma_f32 v[0:1], v[18:19], v[236:237], v[0:1]
	v_pk_fma_f32 v[0:1], v[20:21], v[238:239], v[0:1]
	s_waitcnt vmcnt(4)
	v_mfma_scale_f32_32x32x64_f8f6f4 v[2:17], v[42:49], v[122:129], v[2:17], v203, v203 op_sel_hi:[0,0,0]
	ds_read_b128 v[236:239], v202 offset:80
	v_exp_f32_e64 v22, -v22
	v_exp_f32_e64 v23, -v23
	v_exp_f32_e64 v24, -v24
	v_exp_f32_e64 v25, -v25
	v_add_co_u32_e64 v200, s[42:43], v200, v200
	v_add_co_u32_e64 v200, s[48:49], v200, v200
	v_add_co_u32_e64 v200, s[50:51], v200, v200
	v_add_co_u32_e64 v200, s[56:57], v200, v200
	v_pk_add_f32 v[22:23], v[22:23], v[182:183]
	v_pk_add_f32 v[24:25], v[24:25], v[184:185]
	s_mov_b64 exec, s[42:43]
	v_mul_f32_e32 v224, v224, v22
	s_mov_b64 exec, s[48:49]
	v_mul_f32_e32 v225, v225, v23
	s_mov_b64 exec, s[50:51]
	v_mul_f32_e32 v226, v226, v24
	s_mov_b64 exec, s[56:57]
	v_mul_f32_e32 v227, v227, v25
	s_mov_b64 exec, -1
	v_log_f32_e32 v22, v224
	v_log_f32_e32 v23, v225
	v_log_f32_e32 v24, v226
	v_log_f32_e32 v25, v227
	s_waitcnt lgkmcnt(0)
	v_pk_fma_f32 v[0:1], v[22:23], v[236:237], v[0:1]
	v_pk_fma_f32 v[0:1], v[24:25], v[238:239], v[0:1]
	s_waitcnt vmcnt(2)
	v_mfma_scale_f32_32x32x64_f8f6f4 v[2:17], v[50:57], v[114:121], v[2:17], v203, v203 op_sel_hi:[0,0,0]
	ds_read_b128 v[236:239], v202 offset:96
	v_exp_f32_e64 v26, -v26
	v_exp_f32_e64 v27, -v27
	v_exp_f32_e64 v28, -v28
	v_exp_f32_e64 v29, -v29
	v_add_co_u32_e64 v200, s[42:43], v200, v200
	v_add_co_u32_e64 v200, s[48:49], v200, v200
	v_add_co_u32_e64 v200, s[50:51], v200, v200
	v_add_co_u32_e64 v200, s[56:57], v200, v200
	v_pk_add_f32 v[26:27], v[26:27], v[186:187]
	v_pk_add_f32 v[28:29], v[28:29], v[188:189]
	s_mov_b64 exec, s[42:43]
	v_mul_f32_e32 v228, v228, v26
	s_mov_b64 exec, s[48:49]
	v_mul_f32_e32 v229, v229, v27
	s_mov_b64 exec, s[50:51]
	v_mul_f32_e32 v230, v230, v28
	s_mov_b64 exec, s[56:57]
	v_mul_f32_e32 v231, v231, v29
	s_mov_b64 exec, -1
	v_log_f32_e32 v26, v228
	v_log_f32_e32 v27, v229
	v_log_f32_e32 v28, v230
	v_log_f32_e32 v29, v231
	s_waitcnt lgkmcnt(0)
	v_pk_fma_f32 v[0:1], v[26:27], v[236:237], v[0:1]
	v_pk_fma_f32 v[0:1], v[28:29], v[238:239], v[0:1]
	s_waitcnt vmcnt(0)
	v_mfma_scale_f32_32x32x64_f8f6f4 v[2:17], v[58:65], v[98:105], v[2:17], v203, v203 op_sel_hi:[0,0,0]
	ds_read_b128 v[236:239], v202 offset:112
	v_exp_f32_e64 v30, -v30
	v_exp_f32_e64 v31, -v31
	v_exp_f32_e64 v32, -v32
	v_exp_f32_e64 v33, -v33
	v_add_co_u32_e64 v200, s[42:43], v200, v200
	v_add_co_u32_e64 v200, s[48:49], v200, v200
	v_add_co_u32_e64 v200, s[50:51], v200, v200
	v_add_co_u32_e64 v200, s[56:57], v200, v200
	v_pk_add_f32 v[30:31], v[30:31], v[190:191]
	v_pk_add_f32 v[32:33], v[32:33], v[192:193]
	s_mov_b64 exec, s[42:43]
	v_mul_f32_e32 v232, v232, v30
	s_mov_b64 exec, s[48:49]
	v_mul_f32_e32 v233, v233, v31
	s_mov_b64 exec, s[50:51]
	v_mul_f32_e32 v234, v234, v32
	s_mov_b64 exec, s[56:57]
	v_mul_f32_e32 v235, v235, v33
	s_mov_b64 exec, -1
	v_log_f32_e32 v30, v232
	v_log_f32_e32 v31, v233
	v_log_f32_e32 v32, v234
	v_log_f32_e32 v33, v235
	s_waitcnt lgkmcnt(0)
	v_pk_fma_f32 v[0:1], v[30:31], v[236:237], v[0:1]
	v_pk_fma_f32 v[0:1], v[32:33], v[238:239], v[0:1]
	s_branch .Lq2_halfdone
.Lq2_lasthalf:
	s_nop 3
	ds_read_b128 v[236:239], v202 offset:64
	v_exp_f32_e64 v18, -v18
	v_exp_f32_e64 v19, -v19
	v_exp_f32_e64 v20, -v20
	v_exp_f32_e64 v21, -v21
	v_add_co_u32_e64 v200, s[42:43], v200, v200
	v_add_co_u32_e64 v200, s[48:49], v200, v200
	v_add_co_u32_e64 v200, s[50:51], v200, v200
	v_add_co_u32_e64 v200, s[56:57], v200, v200
	v_pk_add_f32 v[18:19], v[18:19], v[178:179]
	v_pk_add_f32 v[20:21], v[20:21], v[180:181]
	s_mov_b64 exec, s[42:43]
	v_mul_f32_e32 v220, v220, v18
	s_mov_b64 exec, s[48:49]
	v_mul_f32_e32 v221, v221, v19
	s_mov_b64 exec, s[50:51]
	v_mul_f32_e32 v222, v222, v20
	s_mov_b64 exec, s[56:57]
	v_mul_f32_e32 v223, v223, v21
	s_mov_b64 exec, -1
	v_log_f32_e32 v18, v220
	v_log_f32_e32 v19, v221
	v_log_f32_e32 v20, v222
	v_log_f32_e32 v21, v223
	s_waitcnt lgkmcnt(0)
	v_pk_fma_f32 v[0:1], v[18:19], v[236:237], v[0:1]
	v_pk_fma_f32 v[0:1], v[20:21], v[238:239], v[0:1]
	ds_read_b128 v[236:239], v202 offset:80
	v_exp_f32_e64 v22, -v22
	v_exp_f32_e64 v23, -v23
	v_exp_f32_e64 v24, -v24
	v_exp_f32_e64 v25, -v25
	v_add_co_u32_e64 v200, s[42:43], v200, v200
	v_add_co_u32_e64 v200, s[48:49], v200, v200
	v_add_co_u32_e64 v200, s[50:51], v200, v200
	v_add_co_u32_e64 v200, s[56:57], v200, v200
	v_pk_add_f32 v[22:23], v[22:23], v[182:183]
	v_pk_add_f32 v[24:25], v[24:25], v[184:185]
	s_mov_b64 exec, s[42:43]
	v_mul_f32_e32 v224, v224, v22
	s_mov_b64 exec, s[48:49]
	v_mul_f32_e32 v225, v225, v23
	s_mov_b64 exec, s[50:51]
	v_mul_f32_e32 v226, v226, v24
	s_mov_b64 exec, s[56:57]
	v_mul_f32_e32 v227, v227, v25
	s_mov_b64 exec, -1
	v_log_f32_e32 v22, v224
	v_log_f32_e32 v23, v225
	v_log_f32_e32 v24, v226
	v_log_f32_e32 v25, v227
	s_waitcnt lgkmcnt(0)
	v_pk_fma_f32 v[0:1], v[22:23], v[236:237], v[0:1]
	v_pk_fma_f32 v[0:1], v[24:25], v[238:239], v[0:1]
	ds_read_b128 v[236:239], v202 offset:96
	v_exp_f32_e64 v26, -v26
	v_exp_f32_e64 v27, -v27
	v_exp_f32_e64 v28, -v28
	v_exp_f32_e64 v29, -v29
	v_add_co_u32_e64 v200, s[42:43], v200, v200
	v_add_co_u32_e64 v200, s[48:49], v200, v200
	v_add_co_u32_e64 v200, s[50:51], v200, v200
	v_add_co_u32_e64 v200, s[56:57], v200, v200
	v_pk_add_f32 v[26:27], v[26:27], v[186:187]
	v_pk_add_f32 v[28:29], v[28:29], v[188:189]
	s_mov_b64 exec, s[42:43]
	v_mul_f32_e32 v228, v228, v26
	s_mov_b64 exec, s[48:49]
	v_mul_f32_e32 v229, v229, v27
	s_mov_b64 exec, s[50:51]
	v_mul_f32_e32 v230, v230, v28
	s_mov_b64 exec, s[56:57]
	v_mul_f32_e32 v231, v231, v29
	s_mov_b64 exec, -1
	v_log_f32_e32 v26, v228
	v_log_f32_e32 v27, v229
	v_log_f32_e32 v28, v230
	v_log_f32_e32 v29, v231
	s_waitcnt lgkmcnt(0)
	v_pk_fma_f32 v[0:1], v[26:27], v[236:237], v[0:1]
	v_pk_fma_f32 v[0:1], v[28:29], v[238:239], v[0:1]
	ds_read_b128 v[236:239], v202 offset:112
	v_exp_f32_e64 v30, -v30
	v_exp_f32_e64 v31, -v31
	v_exp_f32_e64 v32, -v32
	v_exp_f32_e64 v33, -v33
	v_add_co_u32_e64 v200, s[42:43], v200, v200
	v_add_co_u32_e64 v200, s[48:49], v200, v200
	v_add_co_u32_e64 v200, s[50:51], v200, v200
	v_add_co_u32_e64 v200, s[56:57], v200, v200
	v_pk_add_f32 v[30:31], v[30:31], v[190:191]
	v_pk_add_f32 v[32:33], v[32:33], v[192:193]
	s_mov_b64 exec, s[42:43]
	v_mul_f32_e32 v232, v232, v30
	s_mov_b64 exec, s[48:49]
	v_mul_f32_e32 v233, v233, v31
	s_mov_b64 exec, s[50:51]
	v_mul_f32_e32 v234, v234, v32
	s_mov_b64 exec, s[56:57]
	v_mul_f32_e32 v235, v235, v33
	s_mov_b64 exec, -1
	v_log_f32_e32 v30, v232
	v_log_f32_e32 v31, v233
	v_log_f32_e32 v32, v234
	v_log_f32_e32 v33, v235
	s_waitcnt lgkmcnt(0)
	v_pk_fma_f32 v[0:1], v[30:31], v[236:237], v[0:1]
	v_pk_fma_f32 v[0:1], v[32:33], v[238:239], v[0:1]
